# value-residual GEMM epilogue: the four row loads of a row group (z and v_first, both column halves) issued together behind one wait instead of three serialized round trips
# speedup vs baseline: 1.0009x; 1.0009x over previous
; __device__ __forceinline__ void unpk8(const u32x4 w, f32x4& a, f32x4& b) { a = (f32x4){bflo(w.x), bfhi(w.x), bflo(w.y), bfhi(w.y)}; b = (f32x4){bflo(w.z), bfhi(w.z), bflo(w.w), bfhi(w.w)}; }
; __device__ __forceinline__ u32x4 pk8(const f32x4 a, const f32x4 b) { u32x4 w; w.x = cvt_pk_bf16(a[0], a[1]); w.y = cvt_pk_bf16(a[2], a[3]); w.z = cvt_pk_bf16(b[0], b[1]); w.w = cvt_pk_bf16(b[2], b[3]); return w; }
;     __device__ __forceinline__ void operator()(const f32x4 (&acc)[2][2][4][2], const Unit& u, int wr, int wc, int fr, int fq) const {
;         const int row0 = u.pm * BM + wr * 64 + fr, col0 = u.pn * 256 + wc * 32 + 8 * fq;
;         f32x4 bv[2][2];
; #pragma unroll
;         for (int bj = 0; bj < 2; ++bj)
; #pragma unroll
;             for (int n = 0; n < 2; ++n) bv[bj][n] = *(const f32x4*)(v0b + col0 + bj * HALF + 4 * n);
;         EPI_ROWS_BEGIN
; #pragma unroll
;             for (int bj = 0; bj < 2; ++bj) { bf16_t* zp = zrkv + row * 3072 + 2048 + col0 + bj * HALF;
;                 f32x4 z0, z1, f0, f1; unpk8(*(const u32x4*)zp, z0, z1); unpk8(*(const u32x4*)(vf + row * 1024 + col0 + bj * HALF), f0, f1);
;                 const f32x4 m0 = act4(acc[ai][bj][m][0] + bv[bj][0], 2), m1 = act4(acc[ai][bj][m][1] + bv[bj][1], 2);
;                 *(u32x4*)zp = pk8(z0 + (f0 - z0) * m0, z1 + (f1 - z1) * m1); }
;         EPI_ROWS_END
;     }
.LBB0_767:
	v_lshl_or_b32 v158, s82, 8, v177
	v_ashrrev_i32_e32 v159, 31, v158
	v_lshl_add_u64 v[22:23], v[158:159], 2, s[52:53]
	global_load_dwordx4 v[34:37], v[22:23], off offset:16
	global_load_dwordx4 v[42:45], v[22:23], off
	global_load_dwordx4 v[18:21], v[22:23], off offset:528
	s_nop 0
	global_load_dwordx4 v[22:25], v[22:23], off offset:512
	v_lshl_add_u32 v162, s48, 8, v1
	v_mov_b64_e32 v[160:161], s[54:55]
	s_movk_i32 s27, 0x1800
	v_ashrrev_i32_e32 v163, 31, v162
	v_mad_i64_i32 v[164:165], s[60:61], v162, s27, v[160:161]
	v_lshlrev_b64 v[158:159], 1, v[158:159]
	v_lshlrev_b64 v[166:167], 11, v[162:163]
	v_lshl_add_u64 v[164:165], v[164:165], 0, v[158:159]
	v_add_co_u32_e32 v164, vcc, s9, v164
	v_lshl_add_u64 v[166:167], s[56:57], 0, v[166:167]
	s_nop 0
	v_addc_co_u32_e32 v165, vcc, 0, v165, vcc
	v_lshl_add_u64 v[166:167], v[166:167], 0, v[158:159]
	global_load_dwordx4 v[168:171], v[164:165], off
	global_load_dwordx4 v[180:183], v[166:167], off
	global_load_dwordx4 v[190:193], v[164:165], off offset:256
	global_load_dwordx4 v[194:197], v[166:167], off offset:256
	s_waitcnt vmcnt(0)
	v_pk_add_f32 v[140:141], v[140:141], v[36:37]
	v_pk_add_f32 v[144:145], v[144:145], v[44:45]
	v_pk_add_f32 v[142:143], v[142:143], v[42:43]
	v_mul_f32_e32 v144, 0xbfb8aa3b, v144
	v_mul_f32_e32 v142, 0xbfb8aa3b, v142
	v_mul_f32_e32 v143, 0xbfb8aa3b, v143
	v_mul_f32_e32 v145, 0xbfb8aa3b, v145
	v_pk_add_f32 v[138:139], v[138:139], v[34:35]
	v_exp_f32_e32 v142, v142
	v_exp_f32_e32 v143, v143
	v_exp_f32_e32 v144, v144
	v_exp_f32_e32 v145, v145
	v_mul_f32_e32 v138, 0xbfb8aa3b, v138
	v_mul_f32_e32 v139, 0xbfb8aa3b, v139
	v_mul_f32_e32 v140, 0xbfb8aa3b, v140
	v_mul_f32_e32 v141, 0xbfb8aa3b, v141
	v_exp_f32_e32 v138, v138
	v_exp_f32_e32 v139, v139
	v_exp_f32_e32 v140, v140
	v_exp_f32_e32 v141, v141
	v_add_f32_e32 v142, 1.0, v142
	v_add_f32_e32 v143, 1.0, v143
	v_add_f32_e32 v144, 1.0, v144
	v_add_f32_e32 v145, 1.0, v145
	v_rcp_f32_e32 v142, v142
	v_rcp_f32_e32 v143, v143
	v_rcp_f32_e32 v144, v144
	v_rcp_f32_e32 v145, v145
	v_add_f32_e32 v138, 1.0, v138
	v_add_f32_e32 v139, 1.0, v139
	v_add_f32_e32 v140, 1.0, v140
	v_add_f32_e32 v141, 1.0, v141
	v_rcp_f32_e32 v138, v138
	v_rcp_f32_e32 v139, v139
	v_rcp_f32_e32 v140, v140
	v_rcp_f32_e32 v141, v141
	v_lshlrev_b32_e32 v172, 16, v168
	v_and_b32_e32 v173, 0xffff0000, v168
	v_lshlrev_b32_e32 v174, 16, v169
	v_and_b32_e32 v175, 0xffff0000, v169
	v_lshlrev_b32_e32 v163, 16, v180
	v_and_b32_e32 v179, 0xffff0000, v180
	v_lshlrev_b32_e32 v184, 16, v181
	v_and_b32_e32 v185, 0xffff0000, v181
	v_lshlrev_b32_e32 v168, 16, v170
	v_and_b32_e32 v169, 0xffff0000, v170
	v_lshlrev_b32_e32 v170, 16, v171
	v_and_b32_e32 v171, 0xffff0000, v171
	v_lshlrev_b32_e32 v186, 16, v182
	v_and_b32_e32 v187, 0xffff0000, v182
	v_lshlrev_b32_e32 v188, 16, v183
	v_and_b32_e32 v189, 0xffff0000, v183
	v_sub_f32_e32 v181, v179, v173
	v_sub_f32_e32 v180, v163, v172
	v_sub_f32_e32 v183, v185, v175
	v_sub_f32_e32 v182, v184, v174
	v_pk_fma_f32 v[144:145], v[144:145], v[182:183], v[174:175]
	v_pk_fma_f32 v[142:143], v[142:143], v[180:181], v[172:173]
	v_sub_f32_e32 v173, v187, v169
	v_sub_f32_e32 v172, v186, v168
	v_sub_f32_e32 v175, v189, v171
	v_sub_f32_e32 v174, v188, v170
	v_pk_fma_f32 v[170:171], v[140:141], v[174:175], v[170:171]
	v_pk_fma_f32 v[140:141], v[138:139], v[172:173], v[168:169]
	v_cvt_pk_bf16_f32 v138, v142, v143
	v_cvt_pk_bf16_f32 v139, v144, v145
	v_pk_add_f32 v[136:137], v[136:137], v[24:25]
	v_cvt_pk_bf16_f32 v140, v140, v141
	v_cvt_pk_bf16_f32 v141, v170, v171
	global_store_dwordx4 v[164:165], v[138:141], off
	v_pk_add_f32 v[134:135], v[134:135], v[22:23]
	v_mul_f32_e32 v136, 0xbfb8aa3b, v136
	v_mul_f32_e32 v134, 0xbfb8aa3b, v134
	v_mul_f32_e32 v135, 0xbfb8aa3b, v135
	v_mul_f32_e32 v137, 0xbfb8aa3b, v137
	v_pk_add_f32 v[132:133], v[132:133], v[20:21]
	v_pk_add_f32 v[130:131], v[130:131], v[18:19]
	v_exp_f32_e32 v134, v134
	v_exp_f32_e32 v135, v135
	v_exp_f32_e32 v136, v136
	v_exp_f32_e32 v137, v137
	v_mul_f32_e32 v130, 0xbfb8aa3b, v130
	v_mul_f32_e32 v131, 0xbfb8aa3b, v131
	v_mul_f32_e32 v132, 0xbfb8aa3b, v132
	v_mul_f32_e32 v133, 0xbfb8aa3b, v133
	v_exp_f32_e32 v130, v130
	v_exp_f32_e32 v131, v131
	v_exp_f32_e32 v132, v132
	v_exp_f32_e32 v133, v133
	v_add_f32_e32 v134, 1.0, v134
	v_add_f32_e32 v135, 1.0, v135
	v_add_f32_e32 v136, 1.0, v136
	v_add_f32_e32 v137, 1.0, v137
	v_rcp_f32_e32 v134, v134
	v_rcp_f32_e32 v135, v135
	v_rcp_f32_e32 v136, v136
	v_rcp_f32_e32 v137, v137
	v_add_f32_e32 v130, 1.0, v130
	v_add_f32_e32 v131, 1.0, v131
	v_add_f32_e32 v132, 1.0, v132
	v_add_f32_e32 v133, 1.0, v133
	v_rcp_f32_e32 v130, v130
	v_rcp_f32_e32 v131, v131
	v_rcp_f32_e32 v132, v132
	v_rcp_f32_e32 v133, v133
	v_pk_add_f32 v[128:129], v[128:129], v[44:45]
	v_pk_add_f32 v[126:127], v[126:127], v[42:43]
	v_mul_f32_e32 v128, 0xbfb8aa3b, v128
	v_mul_f32_e32 v126, 0xbfb8aa3b, v126
	v_mul_f32_e32 v127, 0xbfb8aa3b, v127
	v_mul_f32_e32 v129, 0xbfb8aa3b, v129
	v_pk_add_f32 v[124:125], v[124:125], v[36:37]
	v_pk_add_f32 v[122:123], v[122:123], v[34:35]
	v_exp_f32_e32 v126, v126
	v_exp_f32_e32 v127, v127
	v_exp_f32_e32 v128, v128
	v_exp_f32_e32 v129, v129
	v_mul_f32_e32 v122, 0xbfb8aa3b, v122
	v_mul_f32_e32 v123, 0xbfb8aa3b, v123
	v_mul_f32_e32 v124, 0xbfb8aa3b, v124
	v_mul_f32_e32 v125, 0xbfb8aa3b, v125
	v_exp_f32_e32 v122, v122
	v_exp_f32_e32 v123, v123
	v_exp_f32_e32 v124, v124
	v_exp_f32_e32 v125, v125
	v_add_f32_e32 v126, 1.0, v126
	v_add_f32_e32 v127, 1.0, v127
	v_add_f32_e32 v128, 1.0, v128
	v_add_f32_e32 v129, 1.0, v129
	v_rcp_f32_e32 v126, v126
	v_rcp_f32_e32 v127, v127
	v_rcp_f32_e32 v128, v128
	v_rcp_f32_e32 v129, v129
	v_add_f32_e32 v122, 1.0, v122
; __device__ __forceinline__ void unpk8(const u32x4 w, f32x4& a, f32x4& b) { a = (f32x4){bflo(w.x), bfhi(w.x), bflo(w.y), bfhi(w.y)}; b = (f32x4){bflo(w.z), bfhi(w.z), bflo(w.w), bfhi(w.w)}; }
; __device__ __forceinline__ u32x4 pk8(const f32x4 a, const f32x4 b) { u32x4 w; w.x = cvt_pk_bf16(a[0], a[1]); w.y = cvt_pk_bf16(a[2], a[3]); w.z = cvt_pk_bf16(b[0], b[1]); w.w = cvt_pk_bf16(b[2], b[3]); return w; }
;     __device__ __forceinline__ void operator()(const f32x4 (&acc)[2][2][4][2], const Unit& u, int wr, int wc, int fr, int fq) const {
;     ...
;         EPI_ROWS_BEGIN
; #pragma unroll
;             for (int bj = 0; bj < 2; ++bj) { bf16_t* zp = zrkv + row * 3072 + 2048 + col0 + bj * HALF;
;                 f32x4 z0, z1, f0, f1; unpk8(*(const u32x4*)zp, z0, z1); unpk8(*(const u32x4*)(vf + row * 1024 + col0 + bj * HALF), f0, f1);
;                 const f32x4 m0 = act4(acc[ai][bj][m][0] + bv[bj][0], 2), m1 = act4(acc[ai][bj][m][1] + bv[bj][1], 2);
;                 *(u32x4*)zp = pk8(z0 + (f0 - z0) * m0, z1 + (f1 - z1) * m1); }
;         EPI_ROWS_END
	v_add_f32_e32 v123, 1.0, v123
	v_add_f32_e32 v124, 1.0, v124
	v_add_f32_e32 v125, 1.0, v125
	v_rcp_f32_e32 v122, v122
	v_rcp_f32_e32 v123, v123
	v_rcp_f32_e32 v124, v124
	v_rcp_f32_e32 v125, v125
	v_pk_add_f32 v[120:121], v[120:121], v[24:25]
	v_pk_add_f32 v[118:119], v[118:119], v[22:23]
	v_mul_f32_e32 v120, 0xbfb8aa3b, v120
	v_mul_f32_e32 v118, 0xbfb8aa3b, v118
	v_mul_f32_e32 v119, 0xbfb8aa3b, v119
	v_mul_f32_e32 v121, 0xbfb8aa3b, v121
	v_pk_add_f32 v[116:117], v[116:117], v[20:21]
	v_pk_add_f32 v[114:115], v[114:115], v[18:19]
	v_lshlrev_b32_e32 v142, 16, v190
	v_and_b32_e32 v143, 0xffff0000, v190
	v_lshlrev_b32_e32 v144, 16, v191
	v_and_b32_e32 v145, 0xffff0000, v191
	v_lshlrev_b32_e32 v168, 16, v192
	v_and_b32_e32 v169, 0xffff0000, v192
	v_lshlrev_b32_e32 v170, 16, v193
	v_and_b32_e32 v171, 0xffff0000, v193
	v_exp_f32_e32 v118, v118
	v_exp_f32_e32 v119, v119
	v_exp_f32_e32 v120, v120
	v_exp_f32_e32 v121, v121
	v_mul_f32_e32 v114, 0xbfb8aa3b, v114
	v_mul_f32_e32 v115, 0xbfb8aa3b, v115
	v_mul_f32_e32 v116, 0xbfb8aa3b, v116
	v_mul_f32_e32 v117, 0xbfb8aa3b, v117
	v_exp_f32_e32 v114, v114
	v_exp_f32_e32 v115, v115
	v_exp_f32_e32 v116, v116
	v_exp_f32_e32 v117, v117
	v_add_f32_e32 v118, 1.0, v118
	v_add_f32_e32 v119, 1.0, v119
	v_add_f32_e32 v120, 1.0, v120
	v_add_f32_e32 v121, 1.0, v121
	v_rcp_f32_e32 v118, v118
	v_rcp_f32_e32 v119, v119
	v_rcp_f32_e32 v120, v120
	v_rcp_f32_e32 v121, v121
	v_add_f32_e32 v114, 1.0, v114
	v_add_f32_e32 v115, 1.0, v115
	v_add_f32_e32 v116, 1.0, v116
	v_add_f32_e32 v117, 1.0, v117
	v_rcp_f32_e32 v114, v114
	v_rcp_f32_e32 v115, v115
	v_rcp_f32_e32 v116, v116
	v_rcp_f32_e32 v117, v117
	v_pk_add_f32 v[112:113], v[112:113], v[44:45]
	v_pk_add_f32 v[110:111], v[110:111], v[42:43]
	v_mul_f32_e32 v112, 0xbfb8aa3b, v112
	v_mul_f32_e32 v110, 0xbfb8aa3b, v110
	v_mul_f32_e32 v111, 0xbfb8aa3b, v111
	v_mul_f32_e32 v113, 0xbfb8aa3b, v113
	v_pk_add_f32 v[108:109], v[108:109], v[36:37]
	v_pk_add_f32 v[106:107], v[106:107], v[34:35]
	v_exp_f32_e32 v110, v110
	v_exp_f32_e32 v111, v111
	v_exp_f32_e32 v112, v112
	v_exp_f32_e32 v113, v113
	v_mul_f32_e32 v106, 0xbfb8aa3b, v106
	v_mul_f32_e32 v107, 0xbfb8aa3b, v107
	v_mul_f32_e32 v108, 0xbfb8aa3b, v108
	v_mul_f32_e32 v109, 0xbfb8aa3b, v109
	v_exp_f32_e32 v106, v106
	v_exp_f32_e32 v107, v107
	v_exp_f32_e32 v108, v108
	v_exp_f32_e32 v109, v109
	v_add_f32_e32 v110, 1.0, v110
	v_add_f32_e32 v111, 1.0, v111
	v_add_f32_e32 v112, 1.0, v112
	v_add_f32_e32 v113, 1.0, v113
	v_rcp_f32_e32 v110, v110
	v_rcp_f32_e32 v111, v111
	v_rcp_f32_e32 v112, v112
	v_rcp_f32_e32 v113, v113
	v_add_f32_e32 v106, 1.0, v106
	v_add_f32_e32 v107, 1.0, v107
	v_add_f32_e32 v108, 1.0, v108
	v_add_f32_e32 v109, 1.0, v109
	v_rcp_f32_e32 v106, v106
	v_rcp_f32_e32 v107, v107
	v_rcp_f32_e32 v108, v108
	v_rcp_f32_e32 v109, v109
	v_pk_add_f32 v[104:105], v[104:105], v[24:25]
	v_pk_add_f32 v[102:103], v[102:103], v[22:23]
	v_mul_f32_e32 v104, 0xbfb8aa3b, v104
	v_mul_f32_e32 v102, 0xbfb8aa3b, v102
	v_mul_f32_e32 v103, 0xbfb8aa3b, v103
	v_mul_f32_e32 v105, 0xbfb8aa3b, v105
	v_pk_add_f32 v[100:101], v[100:101], v[20:21]
	v_pk_add_f32 v[98:99], v[98:99], v[18:19]
	v_exp_f32_e32 v102, v102
	v_exp_f32_e32 v103, v103
	v_exp_f32_e32 v104, v104
	v_exp_f32_e32 v105, v105
	v_mul_f32_e32 v98, 0xbfb8aa3b, v98
	v_mul_f32_e32 v99, 0xbfb8aa3b, v99
	v_mul_f32_e32 v100, 0xbfb8aa3b, v100
	v_lshlrev_b32_e32 v163, 16, v194
	v_and_b32_e32 v138, 0xffff0000, v194
	v_lshlrev_b32_e32 v166, 16, v195
	v_and_b32_e32 v167, 0xffff0000, v195
	v_lshlrev_b32_e32 v172, 16, v196
	v_and_b32_e32 v173, 0xffff0000, v196
	v_lshlrev_b32_e32 v174, 16, v197
	v_and_b32_e32 v175, 0xffff0000, v197
	v_sub_f32_e32 v139, v138, v143
	v_sub_f32_e32 v138, v163, v142
	v_sub_f32_e32 v141, v167, v145
	v_sub_f32_e32 v140, v166, v144
	v_pk_fma_f32 v[136:137], v[136:137], v[140:141], v[144:145]
	v_pk_fma_f32 v[134:135], v[134:135], v[138:139], v[142:143]
	v_sub_f32_e32 v139, v173, v169
	v_sub_f32_e32 v138, v172, v168
	v_sub_f32_e32 v141, v175, v171
	v_sub_f32_e32 v140, v174, v170
	v_pk_fma_f32 v[140:141], v[132:133], v[140:141], v[170:171]
	v_pk_fma_f32 v[132:133], v[130:131], v[138:139], v[168:169]
	v_cvt_pk_bf16_f32 v130, v134, v135
	v_cvt_pk_bf16_f32 v131, v136, v137
	v_mul_f32_e32 v101, 0xbfb8aa3b, v101
	v_cvt_pk_bf16_f32 v132, v132, v133
	v_cvt_pk_bf16_f32 v133, v140, v141
	global_store_dwordx4 v[164:165], v[130:133], off offset:256
	v_exp_f32_e32 v98, v98
	v_exp_f32_e32 v99, v99
	v_or_b32_e32 v130, 16, v162
	v_ashrrev_i32_e32 v131, 31, v130
	v_lshlrev_b64 v[132:133], 11, v[130:131]
	v_mad_i64_i32 v[130:131], s[60:61], v130, s27, v[160:161]
	v_lshl_add_u64 v[130:131], v[130:131], 0, v[158:159]
	v_add_co_u32_e32 v130, vcc, s9, v130
	v_lshl_add_u64 v[132:133], s[56:57], 0, v[132:133]
	s_nop 0
	v_addc_co_u32_e32 v131, vcc, 0, v131, vcc
	v_lshl_add_u64 v[132:133], v[132:133], 0, v[158:159]
	global_load_dwordx4 v[134:137], v[130:131], off
	global_load_dwordx4 v[142:145], v[132:133], off
	global_load_dwordx4 v[190:193], v[130:131], off offset:256
	global_load_dwordx4 v[194:197], v[132:133], off offset:256
	v_exp_f32_e32 v100, v100
	v_exp_f32_e32 v101, v101
	v_add_f32_e32 v102, 1.0, v102
	v_add_f32_e32 v103, 1.0, v103
	v_add_f32_e32 v104, 1.0, v104
	v_add_f32_e32 v105, 1.0, v105
	v_rcp_f32_e32 v102, v102
	v_rcp_f32_e32 v103, v103
	v_rcp_f32_e32 v104, v104
	v_rcp_f32_e32 v105, v105
	v_add_f32_e32 v98, 1.0, v98
	v_add_f32_e32 v99, 1.0, v99
	v_add_f32_e32 v100, 1.0, v100
	v_add_f32_e32 v101, 1.0, v101
	v_rcp_f32_e32 v98, v98
	v_rcp_f32_e32 v99, v99
	v_rcp_f32_e32 v100, v100
	v_rcp_f32_e32 v101, v101
	v_pk_add_f32 v[96:97], v[96:97], v[44:45]
	v_pk_add_f32 v[94:95], v[94:95], v[42:43]
; __device__ __forceinline__ void unpk8(const u32x4 w, f32x4& a, f32x4& b) { a = (f32x4){bflo(w.x), bfhi(w.x), bflo(w.y), bfhi(w.y)}; b = (f32x4){bflo(w.z), bfhi(w.z), bflo(w.w), bfhi(w.w)}; }
; __device__ __forceinline__ u32x4 pk8(const f32x4 a, const f32x4 b) { u32x4 w; w.x = cvt_pk_bf16(a[0], a[1]); w.y = cvt_pk_bf16(a[2], a[3]); w.z = cvt_pk_bf16(b[0], b[1]); w.w = cvt_pk_bf16(b[2], b[3]); return w; }
;     __device__ __forceinline__ void operator()(const f32x4 (&acc)[2][2][4][2], const Unit& u, int wr, int wc, int fr, int fq) const {
;     ...
;         EPI_ROWS_BEGIN
; #pragma unroll
;             for (int bj = 0; bj < 2; ++bj) { bf16_t* zp = zrkv + row * 3072 + 2048 + col0 + bj * HALF;
;                 f32x4 z0, z1, f0, f1; unpk8(*(const u32x4*)zp, z0, z1); unpk8(*(const u32x4*)(vf + row * 1024 + col0 + bj * HALF), f0, f1);
;                 const f32x4 m0 = act4(acc[ai][bj][m][0] + bv[bj][0], 2), m1 = act4(acc[ai][bj][m][1] + bv[bj][1], 2);
;                 *(u32x4*)zp = pk8(z0 + (f0 - z0) * m0, z1 + (f1 - z1) * m1); }
;         EPI_ROWS_END
	v_mul_f32_e32 v96, 0xbfb8aa3b, v96
	v_mul_f32_e32 v94, 0xbfb8aa3b, v94
	v_mul_f32_e32 v95, 0xbfb8aa3b, v95
	v_mul_f32_e32 v97, 0xbfb8aa3b, v97
	v_pk_add_f32 v[92:93], v[92:93], v[36:37]
	v_pk_add_f32 v[90:91], v[90:91], v[34:35]
	v_exp_f32_e32 v94, v94
	v_exp_f32_e32 v95, v95
	v_exp_f32_e32 v96, v96
	v_exp_f32_e32 v97, v97
	v_mul_f32_e32 v90, 0xbfb8aa3b, v90
	v_mul_f32_e32 v91, 0xbfb8aa3b, v91
	v_mul_f32_e32 v92, 0xbfb8aa3b, v92
	v_mul_f32_e32 v93, 0xbfb8aa3b, v93
	v_exp_f32_e32 v90, v90
	v_exp_f32_e32 v91, v91
	v_exp_f32_e32 v92, v92
	v_exp_f32_e32 v93, v93
	v_add_f32_e32 v94, 1.0, v94
	v_add_f32_e32 v95, 1.0, v95
	v_add_f32_e32 v96, 1.0, v96
	v_add_f32_e32 v97, 1.0, v97
	v_rcp_f32_e32 v94, v94
	v_rcp_f32_e32 v95, v95
	v_rcp_f32_e32 v96, v96
	v_rcp_f32_e32 v97, v97
	v_add_f32_e32 v90, 1.0, v90
	v_add_f32_e32 v91, 1.0, v91
	v_add_f32_e32 v92, 1.0, v92
	v_add_f32_e32 v93, 1.0, v93
	v_rcp_f32_e32 v90, v90
	v_rcp_f32_e32 v91, v91
	v_rcp_f32_e32 v92, v92
	v_rcp_f32_e32 v93, v93
	v_pk_add_f32 v[88:89], v[88:89], v[24:25]
	v_pk_add_f32 v[86:87], v[86:87], v[22:23]
	v_mul_f32_e32 v88, 0xbfb8aa3b, v88
	v_mul_f32_e32 v86, 0xbfb8aa3b, v86
	v_mul_f32_e32 v87, 0xbfb8aa3b, v87
	v_mul_f32_e32 v89, 0xbfb8aa3b, v89
	v_pk_add_f32 v[84:85], v[84:85], v[20:21]
	v_pk_add_f32 v[82:83], v[82:83], v[18:19]
	v_exp_f32_e32 v86, v86
	v_exp_f32_e32 v87, v87
	v_exp_f32_e32 v88, v88
	v_exp_f32_e32 v89, v89
	v_mul_f32_e32 v82, 0xbfb8aa3b, v82
	v_mul_f32_e32 v83, 0xbfb8aa3b, v83
	v_mul_f32_e32 v84, 0xbfb8aa3b, v84
	v_mul_f32_e32 v85, 0xbfb8aa3b, v85
	v_exp_f32_e32 v82, v82
	v_exp_f32_e32 v83, v83
	v_exp_f32_e32 v84, v84
	v_exp_f32_e32 v85, v85
	v_add_f32_e32 v86, 1.0, v86
	v_add_f32_e32 v87, 1.0, v87
	v_add_f32_e32 v88, 1.0, v88
	v_add_f32_e32 v89, 1.0, v89
	s_waitcnt vmcnt(0)
	v_lshlrev_b32_e32 v138, 16, v134
	v_and_b32_e32 v139, 0xffff0000, v134
	v_lshlrev_b32_e32 v140, 16, v135
	v_and_b32_e32 v141, 0xffff0000, v135
	v_lshlrev_b32_e32 v163, 16, v142
	v_and_b32_e32 v142, 0xffff0000, v142
	v_lshlrev_b32_e32 v164, 16, v143
	v_and_b32_e32 v165, 0xffff0000, v143
	v_lshlrev_b32_e32 v134, 16, v136
	v_and_b32_e32 v135, 0xffff0000, v136
	v_lshlrev_b32_e32 v136, 16, v137
	v_and_b32_e32 v137, 0xffff0000, v137
	v_lshlrev_b32_e32 v166, 16, v144
	v_and_b32_e32 v167, 0xffff0000, v144
	v_lshlrev_b32_e32 v168, 16, v145
	v_and_b32_e32 v169, 0xffff0000, v145
	v_sub_f32_e32 v143, v142, v139
	v_sub_f32_e32 v142, v163, v138
	v_sub_f32_e32 v145, v165, v141
	v_sub_f32_e32 v144, v164, v140
	v_pk_fma_f32 v[128:129], v[128:129], v[144:145], v[140:141]
	v_pk_fma_f32 v[126:127], v[126:127], v[142:143], v[138:139]
	v_sub_f32_e32 v139, v167, v135
	v_sub_f32_e32 v138, v166, v134
	v_sub_f32_e32 v141, v169, v137
	v_sub_f32_e32 v140, v168, v136
	v_pk_fma_f32 v[136:137], v[124:125], v[140:141], v[136:137]
	v_pk_fma_f32 v[124:125], v[122:123], v[138:139], v[134:135]
	v_cvt_pk_bf16_f32 v122, v126, v127
	v_cvt_pk_bf16_f32 v123, v128, v129
	v_rcp_f32_e32 v86, v86
	v_cvt_pk_bf16_f32 v124, v124, v125
	v_cvt_pk_bf16_f32 v125, v136, v137
	global_store_dwordx4 v[130:131], v[122:125], off
	v_rcp_f32_e32 v87, v87
	v_rcp_f32_e32 v88, v88
	v_rcp_f32_e32 v89, v89
	v_add_f32_e32 v82, 1.0, v82
	v_add_f32_e32 v83, 1.0, v83
	v_add_f32_e32 v84, 1.0, v84
	v_add_f32_e32 v85, 1.0, v85
	v_rcp_f32_e32 v82, v82
	v_rcp_f32_e32 v83, v83
	v_rcp_f32_e32 v84, v84
	v_rcp_f32_e32 v85, v85
	v_pk_add_f32 v[80:81], v[80:81], v[44:45]
	v_pk_add_f32 v[78:79], v[78:79], v[42:43]
	v_mul_f32_e32 v80, 0xbfb8aa3b, v80
	v_mul_f32_e32 v78, 0xbfb8aa3b, v78
	v_mul_f32_e32 v79, 0xbfb8aa3b, v79
	v_mul_f32_e32 v81, 0xbfb8aa3b, v81
	v_pk_add_f32 v[76:77], v[76:77], v[36:37]
	v_pk_add_f32 v[74:75], v[74:75], v[34:35]
	v_exp_f32_e32 v78, v78
	v_exp_f32_e32 v79, v79
	v_exp_f32_e32 v80, v80
	v_exp_f32_e32 v81, v81
	v_mul_f32_e32 v74, 0xbfb8aa3b, v74
	v_mul_f32_e32 v75, 0xbfb8aa3b, v75
	v_mul_f32_e32 v76, 0xbfb8aa3b, v76
	v_mul_f32_e32 v77, 0xbfb8aa3b, v77
	v_exp_f32_e32 v74, v74
	v_exp_f32_e32 v75, v75
	v_exp_f32_e32 v76, v76
	v_exp_f32_e32 v77, v77
	v_add_f32_e32 v78, 1.0, v78
	v_add_f32_e32 v79, 1.0, v79
	v_add_f32_e32 v80, 1.0, v80
	v_add_f32_e32 v81, 1.0, v81
	v_rcp_f32_e32 v78, v78
	v_rcp_f32_e32 v79, v79
	v_rcp_f32_e32 v80, v80
	v_rcp_f32_e32 v81, v81
	v_add_f32_e32 v74, 1.0, v74
	v_add_f32_e32 v75, 1.0, v75
	v_add_f32_e32 v76, 1.0, v76
	v_add_f32_e32 v77, 1.0, v77
	v_rcp_f32_e32 v74, v74
	v_rcp_f32_e32 v75, v75
	v_rcp_f32_e32 v76, v76
	v_rcp_f32_e32 v77, v77
	v_pk_add_f32 v[72:73], v[72:73], v[24:25]
	v_pk_add_f32 v[70:71], v[70:71], v[22:23]
	v_mul_f32_e32 v72, 0xbfb8aa3b, v72
	v_mul_f32_e32 v70, 0xbfb8aa3b, v70
	v_mul_f32_e32 v71, 0xbfb8aa3b, v71
	v_mul_f32_e32 v73, 0xbfb8aa3b, v73
	v_pk_add_f32 v[68:69], v[68:69], v[20:21]
	v_pk_add_f32 v[66:67], v[66:67], v[18:19]
	v_exp_f32_e32 v70, v70
	v_exp_f32_e32 v71, v71
	v_exp_f32_e32 v72, v72
	v_exp_f32_e32 v73, v73
	v_mul_f32_e32 v66, 0xbfb8aa3b, v66
	v_mul_f32_e32 v67, 0xbfb8aa3b, v67
	v_mul_f32_e32 v68, 0xbfb8aa3b, v68
	v_mul_f32_e32 v69, 0xbfb8aa3b, v69
	v_exp_f32_e32 v66, v66
	v_exp_f32_e32 v67, v67
	v_exp_f32_e32 v68, v68
	v_exp_f32_e32 v69, v69
	v_add_f32_e32 v70, 1.0, v70
	v_add_f32_e32 v71, 1.0, v71
	v_add_f32_e32 v72, 1.0, v72
	v_add_f32_e32 v73, 1.0, v73
	v_rcp_f32_e32 v70, v70
	v_rcp_f32_e32 v71, v71
	v_rcp_f32_e32 v72, v72
	v_rcp_f32_e32 v73, v73
	v_add_f32_e32 v66, 1.0, v66
	v_add_f32_e32 v67, 1.0, v67
	v_add_f32_e32 v68, 1.0, v68
	v_add_f32_e32 v69, 1.0, v69
	v_lshlrev_b32_e32 v126, 16, v190
	v_and_b32_e32 v127, 0xffff0000, v190
	v_lshlrev_b32_e32 v128, 16, v191
	v_and_b32_e32 v129, 0xffff0000, v191
	v_lshlrev_b32_e32 v134, 16, v192
	v_and_b32_e32 v135, 0xffff0000, v192
; __device__ __forceinline__ void unpk8(const u32x4 w, f32x4& a, f32x4& b) { a = (f32x4){bflo(w.x), bfhi(w.x), bflo(w.y), bfhi(w.y)}; b = (f32x4){bflo(w.z), bfhi(w.z), bflo(w.w), bfhi(w.w)}; }
; __device__ __forceinline__ u32x4 pk8(const f32x4 a, const f32x4 b) { u32x4 w; w.x = cvt_pk_bf16(a[0], a[1]); w.y = cvt_pk_bf16(a[2], a[3]); w.z = cvt_pk_bf16(b[0], b[1]); w.w = cvt_pk_bf16(b[2], b[3]); return w; }
;     __device__ __forceinline__ void operator()(const f32x4 (&acc)[2][2][4][2], const Unit& u, int wr, int wc, int fr, int fq) const {
;     ...
;         EPI_ROWS_BEGIN
; #pragma unroll
;             for (int bj = 0; bj < 2; ++bj) { bf16_t* zp = zrkv + row * 3072 + 2048 + col0 + bj * HALF;
;                 f32x4 z0, z1, f0, f1; unpk8(*(const u32x4*)zp, z0, z1); unpk8(*(const u32x4*)(vf + row * 1024 + col0 + bj * HALF), f0, f1);
;                 const f32x4 m0 = act4(acc[ai][bj][m][0] + bv[bj][0], 2), m1 = act4(acc[ai][bj][m][1] + bv[bj][1], 2);
;                 *(u32x4*)zp = pk8(z0 + (f0 - z0) * m0, z1 + (f1 - z1) * m1); }
;         EPI_ROWS_END
	v_lshlrev_b32_e32 v136, 16, v193
	v_and_b32_e32 v137, 0xffff0000, v193
	v_rcp_f32_e32 v66, v66
	v_rcp_f32_e32 v67, v67
	v_rcp_f32_e32 v68, v68
	v_rcp_f32_e32 v69, v69
	v_pk_add_f32 v[64:65], v[64:65], v[44:45]
	v_pk_add_f32 v[62:63], v[62:63], v[42:43]
	v_mul_f32_e32 v64, 0xbfb8aa3b, v64
	v_mul_f32_e32 v62, 0xbfb8aa3b, v62
	v_mul_f32_e32 v63, 0xbfb8aa3b, v63
	v_mul_f32_e32 v65, 0xbfb8aa3b, v65
	v_pk_add_f32 v[60:61], v[60:61], v[36:37]
	v_pk_add_f32 v[58:59], v[58:59], v[34:35]
	v_exp_f32_e32 v62, v62
	v_exp_f32_e32 v63, v63
	v_exp_f32_e32 v64, v64
	v_exp_f32_e32 v65, v65
	v_mul_f32_e32 v58, 0xbfb8aa3b, v58
	v_mul_f32_e32 v59, 0xbfb8aa3b, v59
	v_mul_f32_e32 v60, 0xbfb8aa3b, v60
	v_mul_f32_e32 v61, 0xbfb8aa3b, v61
	v_exp_f32_e32 v58, v58
	v_exp_f32_e32 v59, v59
	v_exp_f32_e32 v60, v60
	v_exp_f32_e32 v61, v61
	v_add_f32_e32 v62, 1.0, v62
	v_add_f32_e32 v63, 1.0, v63
	v_add_f32_e32 v64, 1.0, v64
	v_add_f32_e32 v65, 1.0, v65
	v_rcp_f32_e32 v62, v62
	v_rcp_f32_e32 v63, v63
	v_rcp_f32_e32 v64, v64
	v_rcp_f32_e32 v65, v65
	v_add_f32_e32 v58, 1.0, v58
	v_add_f32_e32 v59, 1.0, v59
	v_add_f32_e32 v60, 1.0, v60
	v_add_f32_e32 v61, 1.0, v61
	v_rcp_f32_e32 v58, v58
	v_rcp_f32_e32 v59, v59
	v_rcp_f32_e32 v60, v60
	v_rcp_f32_e32 v61, v61
	v_pk_add_f32 v[56:57], v[56:57], v[24:25]
	v_pk_add_f32 v[54:55], v[54:55], v[22:23]
	v_mul_f32_e32 v56, 0xbfb8aa3b, v56
	v_mul_f32_e32 v54, 0xbfb8aa3b, v54
	v_mul_f32_e32 v55, 0xbfb8aa3b, v55
	v_mul_f32_e32 v57, 0xbfb8aa3b, v57
	v_pk_add_f32 v[52:53], v[52:53], v[20:21]
	v_pk_add_f32 v[50:51], v[50:51], v[18:19]
	v_exp_f32_e32 v54, v54
	v_exp_f32_e32 v55, v55
	v_exp_f32_e32 v56, v56
	v_exp_f32_e32 v57, v57
	v_mul_f32_e32 v50, 0xbfb8aa3b, v50
	v_mul_f32_e32 v51, 0xbfb8aa3b, v51
	v_mul_f32_e32 v52, 0xbfb8aa3b, v52
	v_mul_f32_e32 v53, 0xbfb8aa3b, v53
	v_exp_f32_e32 v50, v50
	v_exp_f32_e32 v51, v51
	v_exp_f32_e32 v52, v52
	v_exp_f32_e32 v53, v53
	v_add_f32_e32 v54, 1.0, v54
	v_add_f32_e32 v55, 1.0, v55
	v_add_f32_e32 v56, 1.0, v56
	v_add_f32_e32 v57, 1.0, v57
	v_rcp_f32_e32 v54, v54
	v_rcp_f32_e32 v55, v55
	v_rcp_f32_e32 v56, v56
	v_rcp_f32_e32 v57, v57
	v_add_f32_e32 v50, 1.0, v50
	v_add_f32_e32 v51, 1.0, v51
	v_add_f32_e32 v52, 1.0, v52
	v_add_f32_e32 v53, 1.0, v53
	v_rcp_f32_e32 v50, v50
	v_rcp_f32_e32 v51, v51
	v_rcp_f32_e32 v52, v52
	v_rcp_f32_e32 v53, v53
	v_pk_add_f32 v[48:49], v[48:49], v[44:45]
	v_pk_add_f32 v[46:47], v[46:47], v[42:43]
	v_mul_f32_e32 v48, 0xbfb8aa3b, v48
	v_lshlrev_b32_e32 v132, 16, v194
	v_and_b32_e32 v122, 0xffff0000, v194
	v_lshlrev_b32_e32 v133, 16, v195
	v_and_b32_e32 v138, 0xffff0000, v195
	v_lshlrev_b32_e32 v139, 16, v196
	v_and_b32_e32 v140, 0xffff0000, v196
	v_lshlrev_b32_e32 v141, 16, v197
	v_and_b32_e32 v142, 0xffff0000, v197
	v_sub_f32_e32 v123, v122, v127
	v_sub_f32_e32 v122, v132, v126
	v_sub_f32_e32 v125, v138, v129
	v_sub_f32_e32 v124, v133, v128
	v_pk_fma_f32 v[120:121], v[120:121], v[124:125], v[128:129]
	v_pk_fma_f32 v[118:119], v[118:119], v[122:123], v[126:127]
	v_sub_f32_e32 v123, v140, v135
	v_sub_f32_e32 v122, v139, v134
	v_sub_f32_e32 v125, v142, v137
	v_sub_f32_e32 v124, v141, v136
	v_pk_fma_f32 v[124:125], v[116:117], v[124:125], v[136:137]
	v_pk_fma_f32 v[116:117], v[114:115], v[122:123], v[134:135]
	v_cvt_pk_bf16_f32 v114, v118, v119
	v_cvt_pk_bf16_f32 v115, v120, v121
	v_mul_f32_e32 v46, 0xbfb8aa3b, v46
	v_cvt_pk_bf16_f32 v116, v116, v117
	v_cvt_pk_bf16_f32 v117, v124, v125
	global_store_dwordx4 v[130:131], v[114:117], off offset:256
	v_mul_f32_e32 v47, 0xbfb8aa3b, v47
	v_mul_f32_e32 v49, 0xbfb8aa3b, v49
	v_or_b32_e32 v114, 32, v162
	v_ashrrev_i32_e32 v115, 31, v114
	v_lshlrev_b64 v[116:117], 11, v[114:115]
	v_mad_i64_i32 v[114:115], s[60:61], v114, s27, v[160:161]
	v_lshl_add_u64 v[114:115], v[114:115], 0, v[158:159]
	v_add_co_u32_e32 v114, vcc, s9, v114
	v_lshl_add_u64 v[116:117], s[56:57], 0, v[116:117]
	s_nop 0
	v_addc_co_u32_e32 v115, vcc, 0, v115, vcc
	v_lshl_add_u64 v[116:117], v[116:117], 0, v[158:159]
	global_load_dwordx4 v[118:121], v[114:115], off
	global_load_dwordx4 v[126:129], v[116:117], off
	global_load_dwordx4 v[190:193], v[114:115], off offset:256
	global_load_dwordx4 v[194:197], v[116:117], off offset:256
	v_pk_add_f32 v[40:41], v[40:41], v[36:37]
	v_pk_add_f32 v[38:39], v[38:39], v[34:35]
	v_exp_f32_e32 v46, v46
	v_exp_f32_e32 v47, v47
	v_exp_f32_e32 v48, v48
	v_exp_f32_e32 v49, v49
	v_mul_f32_e32 v38, 0xbfb8aa3b, v38
	v_mul_f32_e32 v39, 0xbfb8aa3b, v39
	v_mul_f32_e32 v40, 0xbfb8aa3b, v40
	v_mul_f32_e32 v41, 0xbfb8aa3b, v41
	v_exp_f32_e32 v38, v38
	v_exp_f32_e32 v39, v39
	v_exp_f32_e32 v40, v40
	v_exp_f32_e32 v41, v41
	v_add_f32_e32 v46, 1.0, v46
	v_add_f32_e32 v47, 1.0, v47
	v_add_f32_e32 v48, 1.0, v48
	v_add_f32_e32 v49, 1.0, v49
	v_rcp_f32_e32 v46, v46
	v_rcp_f32_e32 v47, v47
	v_rcp_f32_e32 v48, v48
	v_rcp_f32_e32 v49, v49
	v_add_f32_e32 v38, 1.0, v38
	v_add_f32_e32 v39, 1.0, v39
	v_add_f32_e32 v40, 1.0, v40
	v_add_f32_e32 v41, 1.0, v41
	v_rcp_f32_e32 v38, v38
	v_rcp_f32_e32 v39, v39
	v_rcp_f32_e32 v40, v40
	v_rcp_f32_e32 v41, v41
	v_pk_add_f32 v[32:33], v[32:33], v[24:25]
	v_pk_add_f32 v[30:31], v[30:31], v[22:23]
	v_mul_f32_e32 v32, 0xbfb8aa3b, v32
	v_mul_f32_e32 v30, 0xbfb8aa3b, v30
	v_mul_f32_e32 v31, 0xbfb8aa3b, v31
	v_mul_f32_e32 v33, 0xbfb8aa3b, v33
	v_pk_add_f32 v[28:29], v[28:29], v[20:21]
	v_pk_add_f32 v[26:27], v[26:27], v[18:19]
	v_exp_f32_e32 v30, v30
	v_exp_f32_e32 v31, v31
	v_exp_f32_e32 v32, v32
	v_exp_f32_e32 v33, v33
	v_mul_f32_e32 v26, 0xbfb8aa3b, v26
	v_mul_f32_e32 v27, 0xbfb8aa3b, v27
	v_mul_f32_e32 v28, 0xbfb8aa3b, v28
	v_mul_f32_e32 v29, 0xbfb8aa3b, v29
	v_exp_f32_e32 v26, v26
	v_exp_f32_e32 v27, v27
	v_exp_f32_e32 v28, v28
	v_exp_f32_e32 v29, v29
	v_add_f32_e32 v30, 1.0, v30
	v_add_f32_e32 v31, 1.0, v31
	v_add_f32_e32 v32, 1.0, v32
	v_add_f32_e32 v33, 1.0, v33
	v_rcp_f32_e32 v30, v30
	v_rcp_f32_e32 v31, v31
	v_rcp_f32_e32 v32, v32
	v_rcp_f32_e32 v33, v33
	v_add_f32_e32 v26, 1.0, v26
	v_add_f32_e32 v27, 1.0, v27
	v_add_f32_e32 v28, 1.0, v28
	v_add_f32_e32 v29, 1.0, v29
	v_rcp_f32_e32 v26, v26
	v_rcp_f32_e32 v27, v27
	v_rcp_f32_e32 v28, v28
	v_rcp_f32_e32 v29, v29
	v_pk_add_f32 v[16:17], v[16:17], v[44:45]
	v_pk_add_f32 v[14:15], v[14:15], v[42:43]
	v_mul_f32_e32 v16, 0xbfb8aa3b, v16
	v_mul_f32_e32 v14, 0xbfb8aa3b, v14
	v_mul_f32_e32 v15, 0xbfb8aa3b, v15
	v_mul_f32_e32 v17, 0xbfb8aa3b, v17
	v_pk_add_f32 v[12:13], v[12:13], v[36:37]
	v_pk_add_f32 v[10:11], v[10:11], v[34:35]
	v_exp_f32_e32 v14, v14
	v_exp_f32_e32 v15, v15
	v_exp_f32_e32 v16, v16
	v_exp_f32_e32 v17, v17
	s_waitcnt vmcnt(0)
; __device__ __forceinline__ void unpk8(const u32x4 w, f32x4& a, f32x4& b) { a = (f32x4){bflo(w.x), bfhi(w.x), bflo(w.y), bfhi(w.y)}; b = (f32x4){bflo(w.z), bfhi(w.z), bflo(w.w), bfhi(w.w)}; }
; __device__ __forceinline__ u32x4 pk8(const f32x4 a, const f32x4 b) { u32x4 w; w.x = cvt_pk_bf16(a[0], a[1]); w.y = cvt_pk_bf16(a[2], a[3]); w.z = cvt_pk_bf16(b[0], b[1]); w.w = cvt_pk_bf16(b[2], b[3]); return w; }
;     __device__ __forceinline__ void operator()(const f32x4 (&acc)[2][2][4][2], const Unit& u, int wr, int wc, int fr, int fq) const {
;     ...
;         EPI_ROWS_BEGIN
; #pragma unroll
;             for (int bj = 0; bj < 2; ++bj) { bf16_t* zp = zrkv + row * 3072 + 2048 + col0 + bj * HALF;
;                 f32x4 z0, z1, f0, f1; unpk8(*(const u32x4*)zp, z0, z1); unpk8(*(const u32x4*)(vf + row * 1024 + col0 + bj * HALF), f0, f1);
;                 const f32x4 m0 = act4(acc[ai][bj][m][0] + bv[bj][0], 2), m1 = act4(acc[ai][bj][m][1] + bv[bj][1], 2);
;                 *(u32x4*)zp = pk8(z0 + (f0 - z0) * m0, z1 + (f1 - z1) * m1); }
;         EPI_ROWS_END
	v_lshlrev_b32_e32 v122, 16, v118
	v_and_b32_e32 v123, 0xffff0000, v118
	v_lshlrev_b32_e32 v124, 16, v119
	v_and_b32_e32 v125, 0xffff0000, v119
	v_lshlrev_b32_e32 v130, 16, v126
	v_and_b32_e32 v126, 0xffff0000, v126
	v_lshlrev_b32_e32 v131, 16, v127
	v_and_b32_e32 v132, 0xffff0000, v127
	v_lshlrev_b32_e32 v118, 16, v120
	v_and_b32_e32 v119, 0xffff0000, v120
	v_lshlrev_b32_e32 v120, 16, v121
	v_and_b32_e32 v121, 0xffff0000, v121
	v_lshlrev_b32_e32 v133, 16, v128
	v_and_b32_e32 v134, 0xffff0000, v128
	v_lshlrev_b32_e32 v135, 16, v129
	v_and_b32_e32 v136, 0xffff0000, v129
	v_sub_f32_e32 v127, v126, v123
	v_sub_f32_e32 v126, v130, v122
	v_sub_f32_e32 v129, v132, v125
	v_sub_f32_e32 v128, v131, v124
	v_pk_fma_f32 v[112:113], v[112:113], v[128:129], v[124:125]
	v_pk_fma_f32 v[110:111], v[110:111], v[126:127], v[122:123]
	v_sub_f32_e32 v123, v134, v119
	v_sub_f32_e32 v122, v133, v118
	v_sub_f32_e32 v125, v136, v121
	v_sub_f32_e32 v124, v135, v120
	v_pk_fma_f32 v[120:121], v[108:109], v[124:125], v[120:121]
	v_pk_fma_f32 v[108:109], v[106:107], v[122:123], v[118:119]
	v_cvt_pk_bf16_f32 v106, v110, v111
	v_cvt_pk_bf16_f32 v107, v112, v113
	v_mul_f32_e32 v10, 0xbfb8aa3b, v10
	v_cvt_pk_bf16_f32 v108, v108, v109
	v_cvt_pk_bf16_f32 v109, v120, v121
	global_store_dwordx4 v[114:115], v[106:109], off
	v_mul_f32_e32 v11, 0xbfb8aa3b, v11
	v_mul_f32_e32 v12, 0xbfb8aa3b, v12
	v_mul_f32_e32 v13, 0xbfb8aa3b, v13
	v_exp_f32_e32 v10, v10
	v_exp_f32_e32 v11, v11
	v_exp_f32_e32 v12, v12
	v_exp_f32_e32 v13, v13
	v_add_f32_e32 v14, 1.0, v14
	v_add_f32_e32 v15, 1.0, v15
	v_add_f32_e32 v16, 1.0, v16
	v_add_f32_e32 v17, 1.0, v17
	v_rcp_f32_e32 v14, v14
	v_rcp_f32_e32 v15, v15
	v_rcp_f32_e32 v16, v16
	v_rcp_f32_e32 v17, v17
	v_add_f32_e32 v10, 1.0, v10
	v_add_f32_e32 v11, 1.0, v11
	v_add_f32_e32 v12, 1.0, v12
	v_add_f32_e32 v13, 1.0, v13
	v_rcp_f32_e32 v10, v10
	v_rcp_f32_e32 v11, v11
	v_rcp_f32_e32 v12, v12
	v_rcp_f32_e32 v13, v13
	v_pk_add_f32 v[8:9], v[8:9], v[24:25]
	v_pk_add_f32 v[6:7], v[6:7], v[22:23]
	v_mul_f32_e32 v8, 0xbfb8aa3b, v8
	v_mul_f32_e32 v6, 0xbfb8aa3b, v6
	v_mul_f32_e32 v7, 0xbfb8aa3b, v7
	v_mul_f32_e32 v9, 0xbfb8aa3b, v9
	v_pk_add_f32 v[4:5], v[4:5], v[20:21]
	v_pk_add_f32 v[2:3], v[2:3], v[18:19]
	v_exp_f32_e32 v6, v6
	v_exp_f32_e32 v7, v7
	v_exp_f32_e32 v8, v8
	v_exp_f32_e32 v9, v9
	v_mul_f32_e32 v2, 0xbfb8aa3b, v2
	v_mul_f32_e32 v3, 0xbfb8aa3b, v3
	v_mul_f32_e32 v4, 0xbfb8aa3b, v4
	v_mul_f32_e32 v5, 0xbfb8aa3b, v5
	v_exp_f32_e32 v2, v2
	v_exp_f32_e32 v3, v3
	v_exp_f32_e32 v4, v4
	v_exp_f32_e32 v5, v5
	v_add_f32_e32 v6, 1.0, v6
	v_add_f32_e32 v7, 1.0, v7
	v_add_f32_e32 v8, 1.0, v8
	v_add_f32_e32 v9, 1.0, v9
	v_rcp_f32_e32 v6, v6
	v_rcp_f32_e32 v7, v7
	v_rcp_f32_e32 v8, v8
	v_rcp_f32_e32 v9, v9
	v_add_f32_e32 v2, 1.0, v2
	v_add_f32_e32 v3, 1.0, v3
	v_add_f32_e32 v4, 1.0, v4
	v_add_f32_e32 v5, 1.0, v5
	v_rcp_f32_e32 v2, v2
	v_rcp_f32_e32 v3, v3
	v_rcp_f32_e32 v4, v4
	v_rcp_f32_e32 v5, v5
	v_lshlrev_b32_e32 v110, 16, v190
	v_and_b32_e32 v111, 0xffff0000, v190
	v_lshlrev_b32_e32 v112, 16, v191
	v_and_b32_e32 v113, 0xffff0000, v191
	v_lshlrev_b32_e32 v118, 16, v192
	v_and_b32_e32 v119, 0xffff0000, v192
	v_lshlrev_b32_e32 v120, 16, v193
	v_and_b32_e32 v121, 0xffff0000, v193
	v_lshlrev_b32_e32 v116, 16, v194
	v_and_b32_e32 v106, 0xffff0000, v194
	v_lshlrev_b32_e32 v117, 16, v195
	v_and_b32_e32 v122, 0xffff0000, v195
	v_lshlrev_b32_e32 v123, 16, v196
	v_and_b32_e32 v124, 0xffff0000, v196
	v_lshlrev_b32_e32 v125, 16, v197
	v_and_b32_e32 v126, 0xffff0000, v197
	v_sub_f32_e32 v107, v106, v111
	v_sub_f32_e32 v106, v116, v110
	v_sub_f32_e32 v109, v122, v113
	v_sub_f32_e32 v108, v117, v112
	v_pk_fma_f32 v[104:105], v[104:105], v[108:109], v[112:113]
	v_pk_fma_f32 v[102:103], v[102:103], v[106:107], v[110:111]
	v_sub_f32_e32 v107, v124, v119
	v_sub_f32_e32 v106, v123, v118
	v_sub_f32_e32 v109, v126, v121
	v_sub_f32_e32 v108, v125, v120
	v_pk_fma_f32 v[108:109], v[100:101], v[108:109], v[120:121]
	v_pk_fma_f32 v[100:101], v[98:99], v[106:107], v[118:119]
	v_cvt_pk_bf16_f32 v98, v102, v103
	v_cvt_pk_bf16_f32 v99, v104, v105
	s_nop 0
	v_cvt_pk_bf16_f32 v100, v100, v101
	v_cvt_pk_bf16_f32 v101, v108, v109
	global_store_dwordx4 v[114:115], v[98:101], off offset:256
	s_nop 1
	v_or_b32_e32 v98, 48, v162
	v_ashrrev_i32_e32 v99, 31, v98
	v_lshlrev_b64 v[100:101], 11, v[98:99]
	v_mad_i64_i32 v[98:99], s[60:61], v98, s27, v[160:161]
	v_lshl_add_u64 v[98:99], v[98:99], 0, v[158:159]
	v_add_co_u32_e32 v98, vcc, s9, v98
	v_lshl_add_u64 v[100:101], s[56:57], 0, v[100:101]
	s_nop 0
	v_addc_co_u32_e32 v99, vcc, 0, v99, vcc
	v_lshl_add_u64 v[100:101], v[100:101], 0, v[158:159]
	global_load_dwordx4 v[102:105], v[98:99], off
	global_load_dwordx4 v[110:113], v[100:101], off
	global_load_dwordx4 v[190:193], v[98:99], off offset:256
	global_load_dwordx4 v[194:197], v[100:101], off offset:256
	s_waitcnt vmcnt(0)
; __device__ __forceinline__ void unpk8(const u32x4 w, f32x4& a, f32x4& b) { a = (f32x4){bflo(w.x), bfhi(w.x), bflo(w.y), bfhi(w.y)}; b = (f32x4){bflo(w.z), bfhi(w.z), bflo(w.w), bfhi(w.w)}; }
; __device__ __forceinline__ u32x4 pk8(const f32x4 a, const f32x4 b) { u32x4 w; w.x = cvt_pk_bf16(a[0], a[1]); w.y = cvt_pk_bf16(a[2], a[3]); w.z = cvt_pk_bf16(b[0], b[1]); w.w = cvt_pk_bf16(b[2], b[3]); return w; }
;     __device__ __forceinline__ void operator()(const f32x4 (&acc)[2][2][4][2], const Unit& u, int wr, int wc, int fr, int fq) const {
;     ...
;         EPI_ROWS_BEGIN
; #pragma unroll
;             for (int bj = 0; bj < 2; ++bj) { bf16_t* zp = zrkv + row * 3072 + 2048 + col0 + bj * HALF;
;                 f32x4 z0, z1, f0, f1; unpk8(*(const u32x4*)zp, z0, z1); unpk8(*(const u32x4*)(vf + row * 1024 + col0 + bj * HALF), f0, f1);
;                 const f32x4 m0 = act4(acc[ai][bj][m][0] + bv[bj][0], 2), m1 = act4(acc[ai][bj][m][1] + bv[bj][1], 2);
;                 *(u32x4*)zp = pk8(z0 + (f0 - z0) * m0, z1 + (f1 - z1) * m1); }
;         EPI_ROWS_END
	v_lshlrev_b32_e32 v106, 16, v102
	v_and_b32_e32 v107, 0xffff0000, v102
	v_lshlrev_b32_e32 v108, 16, v103
	v_and_b32_e32 v109, 0xffff0000, v103
	v_lshlrev_b32_e32 v114, 16, v110
	v_and_b32_e32 v110, 0xffff0000, v110
	v_lshlrev_b32_e32 v115, 16, v111
	v_and_b32_e32 v116, 0xffff0000, v111
	v_lshlrev_b32_e32 v102, 16, v104
	v_and_b32_e32 v103, 0xffff0000, v104
	v_lshlrev_b32_e32 v104, 16, v105
	v_and_b32_e32 v105, 0xffff0000, v105
	v_lshlrev_b32_e32 v117, 16, v112
	v_and_b32_e32 v118, 0xffff0000, v112
	v_lshlrev_b32_e32 v119, 16, v113
	v_and_b32_e32 v120, 0xffff0000, v113
	v_sub_f32_e32 v111, v110, v107
	v_sub_f32_e32 v110, v114, v106
	v_sub_f32_e32 v113, v116, v109
	v_sub_f32_e32 v112, v115, v108
	v_pk_fma_f32 v[96:97], v[96:97], v[112:113], v[108:109]
	v_pk_fma_f32 v[94:95], v[94:95], v[110:111], v[106:107]
	v_sub_f32_e32 v107, v118, v103
	v_sub_f32_e32 v106, v117, v102
	v_sub_f32_e32 v109, v120, v105
	v_sub_f32_e32 v108, v119, v104
	v_pk_fma_f32 v[104:105], v[92:93], v[108:109], v[104:105]
	v_pk_fma_f32 v[92:93], v[90:91], v[106:107], v[102:103]
	v_cvt_pk_bf16_f32 v90, v94, v95
	v_cvt_pk_bf16_f32 v91, v96, v97
	s_nop 0
	v_cvt_pk_bf16_f32 v92, v92, v93
	v_cvt_pk_bf16_f32 v93, v104, v105
	global_store_dwordx4 v[98:99], v[90:93], off
	v_lshlrev_b32_e32 v94, 16, v190
	v_and_b32_e32 v95, 0xffff0000, v190
	v_lshlrev_b32_e32 v96, 16, v191
	v_and_b32_e32 v97, 0xffff0000, v191
	v_lshlrev_b32_e32 v102, 16, v192
	v_and_b32_e32 v103, 0xffff0000, v192
	v_lshlrev_b32_e32 v104, 16, v193
	v_and_b32_e32 v105, 0xffff0000, v193
	v_lshlrev_b32_e32 v100, 16, v194
	v_and_b32_e32 v90, 0xffff0000, v194
	v_lshlrev_b32_e32 v101, 16, v195
	v_and_b32_e32 v106, 0xffff0000, v195
	v_lshlrev_b32_e32 v107, 16, v196
	v_and_b32_e32 v108, 0xffff0000, v196
	v_lshlrev_b32_e32 v109, 16, v197
	v_and_b32_e32 v110, 0xffff0000, v197
	v_sub_f32_e32 v91, v90, v95
	v_sub_f32_e32 v90, v100, v94
	v_sub_f32_e32 v93, v106, v97
	v_sub_f32_e32 v92, v101, v96
	v_pk_fma_f32 v[88:89], v[88:89], v[92:93], v[96:97]
	v_pk_fma_f32 v[86:87], v[86:87], v[90:91], v[94:95]
	v_sub_f32_e32 v91, v108, v103
	v_sub_f32_e32 v90, v107, v102
	v_sub_f32_e32 v93, v110, v105
	v_sub_f32_e32 v92, v109, v104
	v_pk_fma_f32 v[92:93], v[84:85], v[92:93], v[104:105]
	v_pk_fma_f32 v[84:85], v[82:83], v[90:91], v[102:103]
	v_cvt_pk_bf16_f32 v82, v86, v87
	v_cvt_pk_bf16_f32 v83, v88, v89
	s_nop 0
	v_cvt_pk_bf16_f32 v84, v84, v85
	v_cvt_pk_bf16_f32 v85, v92, v93
	global_store_dwordx4 v[98:99], v[82:85], off offset:256
	s_nop 1
	v_add_u32_e32 v82, 0x80, v162
	v_ashrrev_i32_e32 v83, 31, v82
	v_lshlrev_b64 v[84:85], 11, v[82:83]
	v_mad_i64_i32 v[82:83], s[60:61], v82, s27, v[160:161]
	v_lshl_add_u64 v[82:83], v[82:83], 0, v[158:159]
	v_add_co_u32_e32 v82, vcc, s9, v82
	v_lshl_add_u64 v[84:85], s[56:57], 0, v[84:85]
	s_nop 0
	v_addc_co_u32_e32 v83, vcc, 0, v83, vcc
	v_lshl_add_u64 v[84:85], v[84:85], 0, v[158:159]
	global_load_dwordx4 v[86:89], v[82:83], off
	global_load_dwordx4 v[94:97], v[84:85], off
	global_load_dwordx4 v[190:193], v[82:83], off offset:256
	global_load_dwordx4 v[194:197], v[84:85], off offset:256
	s_waitcnt vmcnt(0)
	v_lshlrev_b32_e32 v90, 16, v86
	v_and_b32_e32 v91, 0xffff0000, v86
	v_lshlrev_b32_e32 v92, 16, v87
	v_and_b32_e32 v93, 0xffff0000, v87
	v_lshlrev_b32_e32 v98, 16, v94
	v_and_b32_e32 v94, 0xffff0000, v94
	v_lshlrev_b32_e32 v99, 16, v95
	v_and_b32_e32 v100, 0xffff0000, v95
	v_lshlrev_b32_e32 v86, 16, v88
	v_and_b32_e32 v87, 0xffff0000, v88
	v_lshlrev_b32_e32 v88, 16, v89
	v_and_b32_e32 v89, 0xffff0000, v89
	v_lshlrev_b32_e32 v101, 16, v96
	v_and_b32_e32 v102, 0xffff0000, v96
	v_lshlrev_b32_e32 v103, 16, v97
	v_and_b32_e32 v104, 0xffff0000, v97
	v_sub_f32_e32 v95, v94, v91
	v_sub_f32_e32 v94, v98, v90
	v_sub_f32_e32 v97, v100, v93
	v_sub_f32_e32 v96, v99, v92
	v_pk_fma_f32 v[80:81], v[80:81], v[96:97], v[92:93]
	v_pk_fma_f32 v[78:79], v[78:79], v[94:95], v[90:91]
	v_sub_f32_e32 v91, v102, v87
	v_sub_f32_e32 v90, v101, v86
	v_sub_f32_e32 v93, v104, v89
	v_sub_f32_e32 v92, v103, v88
	v_pk_fma_f32 v[88:89], v[76:77], v[92:93], v[88:89]
	v_pk_fma_f32 v[76:77], v[74:75], v[90:91], v[86:87]
	v_cvt_pk_bf16_f32 v74, v78, v79
	v_cvt_pk_bf16_f32 v75, v80, v81
	s_nop 0
	v_cvt_pk_bf16_f32 v76, v76, v77
	v_cvt_pk_bf16_f32 v77, v88, v89
	global_store_dwordx4 v[82:83], v[74:77], off
	v_lshlrev_b32_e32 v78, 16, v190
	v_and_b32_e32 v79, 0xffff0000, v190
	v_lshlrev_b32_e32 v80, 16, v191
	v_and_b32_e32 v81, 0xffff0000, v191
	v_lshlrev_b32_e32 v86, 16, v192
	v_and_b32_e32 v87, 0xffff0000, v192
	v_lshlrev_b32_e32 v88, 16, v193
	v_and_b32_e32 v89, 0xffff0000, v193
	v_lshlrev_b32_e32 v84, 16, v194
	v_and_b32_e32 v74, 0xffff0000, v194
	v_lshlrev_b32_e32 v85, 16, v195
	v_and_b32_e32 v90, 0xffff0000, v195
	v_lshlrev_b32_e32 v91, 16, v196
	v_and_b32_e32 v92, 0xffff0000, v196
	v_lshlrev_b32_e32 v93, 16, v197
	v_and_b32_e32 v94, 0xffff0000, v197
	v_sub_f32_e32 v75, v74, v79
	v_sub_f32_e32 v74, v84, v78
	v_sub_f32_e32 v77, v90, v81
	v_sub_f32_e32 v76, v85, v80
	v_pk_fma_f32 v[72:73], v[72:73], v[76:77], v[80:81]
	v_pk_fma_f32 v[70:71], v[70:71], v[74:75], v[78:79]
	v_sub_f32_e32 v75, v92, v87
	v_sub_f32_e32 v74, v91, v86
	v_sub_f32_e32 v77, v94, v89
	v_sub_f32_e32 v76, v93, v88
	v_pk_fma_f32 v[76:77], v[68:69], v[76:77], v[88:89]
	v_pk_fma_f32 v[68:69], v[66:67], v[74:75], v[86:87]
	v_cvt_pk_bf16_f32 v66, v70, v71
	v_cvt_pk_bf16_f32 v67, v72, v73
	s_nop 0
	v_cvt_pk_bf16_f32 v68, v68, v69
	v_cvt_pk_bf16_f32 v69, v76, v77
	global_store_dwordx4 v[82:83], v[66:69], off offset:256
	s_nop 1
	v_add_u32_e32 v66, 0x90, v162
	v_ashrrev_i32_e32 v67, 31, v66
	v_lshlrev_b64 v[68:69], 11, v[66:67]
	v_mad_i64_i32 v[66:67], s[60:61], v66, s27, v[160:161]
	v_lshl_add_u64 v[66:67], v[66:67], 0, v[158:159]
	v_add_co_u32_e32 v66, vcc, s9, v66
	v_lshl_add_u64 v[68:69], s[56:57], 0, v[68:69]
	s_nop 0
	v_addc_co_u32_e32 v67, vcc, 0, v67, vcc
	v_lshl_add_u64 v[68:69], v[68:69], 0, v[158:159]
	global_load_dwordx4 v[70:73], v[66:67], off
	global_load_dwordx4 v[78:81], v[68:69], off
	global_load_dwordx4 v[190:193], v[66:67], off offset:256
	global_load_dwordx4 v[194:197], v[68:69], off offset:256
	s_waitcnt vmcnt(0)
; __device__ __forceinline__ void unpk8(const u32x4 w, f32x4& a, f32x4& b) { a = (f32x4){bflo(w.x), bfhi(w.x), bflo(w.y), bfhi(w.y)}; b = (f32x4){bflo(w.z), bfhi(w.z), bflo(w.w), bfhi(w.w)}; }
; __device__ __forceinline__ u32x4 pk8(const f32x4 a, const f32x4 b) { u32x4 w; w.x = cvt_pk_bf16(a[0], a[1]); w.y = cvt_pk_bf16(a[2], a[3]); w.z = cvt_pk_bf16(b[0], b[1]); w.w = cvt_pk_bf16(b[2], b[3]); return w; }
;     __device__ __forceinline__ void operator()(const f32x4 (&acc)[2][2][4][2], const Unit& u, int wr, int wc, int fr, int fq) const {
;     ...
;         EPI_ROWS_BEGIN
; #pragma unroll
;             for (int bj = 0; bj < 2; ++bj) { bf16_t* zp = zrkv + row * 3072 + 2048 + col0 + bj * HALF;
;                 f32x4 z0, z1, f0, f1; unpk8(*(const u32x4*)zp, z0, z1); unpk8(*(const u32x4*)(vf + row * 1024 + col0 + bj * HALF), f0, f1);
;                 const f32x4 m0 = act4(acc[ai][bj][m][0] + bv[bj][0], 2), m1 = act4(acc[ai][bj][m][1] + bv[bj][1], 2);
;                 *(u32x4*)zp = pk8(z0 + (f0 - z0) * m0, z1 + (f1 - z1) * m1); }
;         EPI_ROWS_END
	v_lshlrev_b32_e32 v74, 16, v70
	v_and_b32_e32 v75, 0xffff0000, v70
	v_lshlrev_b32_e32 v76, 16, v71
	v_and_b32_e32 v77, 0xffff0000, v71
	v_lshlrev_b32_e32 v82, 16, v78
	v_and_b32_e32 v78, 0xffff0000, v78
	v_lshlrev_b32_e32 v83, 16, v79
	v_and_b32_e32 v84, 0xffff0000, v79
	v_lshlrev_b32_e32 v70, 16, v72
	v_and_b32_e32 v71, 0xffff0000, v72
	v_lshlrev_b32_e32 v72, 16, v73
	v_and_b32_e32 v73, 0xffff0000, v73
	v_lshlrev_b32_e32 v85, 16, v80
	v_and_b32_e32 v86, 0xffff0000, v80
	v_lshlrev_b32_e32 v87, 16, v81
	v_and_b32_e32 v88, 0xffff0000, v81
	v_sub_f32_e32 v79, v78, v75
	v_sub_f32_e32 v78, v82, v74
	v_sub_f32_e32 v81, v84, v77
	v_sub_f32_e32 v80, v83, v76
	v_pk_fma_f32 v[64:65], v[64:65], v[80:81], v[76:77]
	v_pk_fma_f32 v[62:63], v[62:63], v[78:79], v[74:75]
	v_sub_f32_e32 v75, v86, v71
	v_sub_f32_e32 v74, v85, v70
	v_sub_f32_e32 v77, v88, v73
	v_sub_f32_e32 v76, v87, v72
	v_pk_fma_f32 v[72:73], v[60:61], v[76:77], v[72:73]
	v_pk_fma_f32 v[60:61], v[58:59], v[74:75], v[70:71]
	v_cvt_pk_bf16_f32 v58, v62, v63
	v_cvt_pk_bf16_f32 v59, v64, v65
	s_nop 0
	v_cvt_pk_bf16_f32 v60, v60, v61
	v_cvt_pk_bf16_f32 v61, v72, v73
	global_store_dwordx4 v[66:67], v[58:61], off
	v_lshlrev_b32_e32 v62, 16, v190
	v_and_b32_e32 v63, 0xffff0000, v190
	v_lshlrev_b32_e32 v64, 16, v191
	v_and_b32_e32 v65, 0xffff0000, v191
	v_lshlrev_b32_e32 v70, 16, v192
	v_and_b32_e32 v71, 0xffff0000, v192
	v_lshlrev_b32_e32 v72, 16, v193
	v_and_b32_e32 v73, 0xffff0000, v193
	v_lshlrev_b32_e32 v68, 16, v194
	v_and_b32_e32 v58, 0xffff0000, v194
	v_lshlrev_b32_e32 v69, 16, v195
	v_and_b32_e32 v74, 0xffff0000, v195
	v_lshlrev_b32_e32 v75, 16, v196
	v_and_b32_e32 v76, 0xffff0000, v196
	v_lshlrev_b32_e32 v77, 16, v197
	v_and_b32_e32 v78, 0xffff0000, v197
	v_sub_f32_e32 v59, v58, v63
	v_sub_f32_e32 v58, v68, v62
	v_sub_f32_e32 v61, v74, v65
	v_sub_f32_e32 v60, v69, v64
	v_pk_fma_f32 v[56:57], v[56:57], v[60:61], v[64:65]
	v_pk_fma_f32 v[54:55], v[54:55], v[58:59], v[62:63]
	v_sub_f32_e32 v59, v76, v71
	v_sub_f32_e32 v58, v75, v70
	v_sub_f32_e32 v61, v78, v73
	v_sub_f32_e32 v60, v77, v72
	v_pk_fma_f32 v[60:61], v[52:53], v[60:61], v[72:73]
	v_pk_fma_f32 v[52:53], v[50:51], v[58:59], v[70:71]
	v_cvt_pk_bf16_f32 v50, v54, v55
	v_cvt_pk_bf16_f32 v51, v56, v57
	s_nop 0
	v_cvt_pk_bf16_f32 v52, v52, v53
	v_cvt_pk_bf16_f32 v53, v60, v61
	global_store_dwordx4 v[66:67], v[50:53], off offset:256
	s_nop 1
	v_add_u32_e32 v50, 0xa0, v162
	v_ashrrev_i32_e32 v51, 31, v50
	v_lshlrev_b64 v[52:53], 11, v[50:51]
	v_mad_i64_i32 v[50:51], s[60:61], v50, s27, v[160:161]
	v_lshl_add_u64 v[50:51], v[50:51], 0, v[158:159]
	v_add_co_u32_e32 v50, vcc, s9, v50
	v_lshl_add_u64 v[52:53], s[56:57], 0, v[52:53]
	s_nop 0
	v_addc_co_u32_e32 v51, vcc, 0, v51, vcc
	v_lshl_add_u64 v[52:53], v[52:53], 0, v[158:159]
	global_load_dwordx4 v[54:57], v[50:51], off
	global_load_dwordx4 v[62:65], v[52:53], off
	global_load_dwordx4 v[190:193], v[50:51], off offset:256
	global_load_dwordx4 v[194:197], v[52:53], off offset:256
	s_waitcnt vmcnt(0)
; __device__ __forceinline__ void unpk8(const u32x4 w, f32x4& a, f32x4& b) { a = (f32x4){bflo(w.x), bfhi(w.x), bflo(w.y), bfhi(w.y)}; b = (f32x4){bflo(w.z), bfhi(w.z), bflo(w.w), bfhi(w.w)}; }
; __device__ __forceinline__ u32x4 pk8(const f32x4 a, const f32x4 b) { u32x4 w; w.x = cvt_pk_bf16(a[0], a[1]); w.y = cvt_pk_bf16(a[2], a[3]); w.z = cvt_pk_bf16(b[0], b[1]); w.w = cvt_pk_bf16(b[2], b[3]); return w; }
;     __device__ __forceinline__ void operator()(const f32x4 (&acc)[2][2][4][2], const Unit& u, int wr, int wc, int fr, int fq) const {
;     ...
;         EPI_ROWS_BEGIN
; #pragma unroll
;             for (int bj = 0; bj < 2; ++bj) { bf16_t* zp = zrkv + row * 3072 + 2048 + col0 + bj * HALF;
;                 f32x4 z0, z1, f0, f1; unpk8(*(const u32x4*)zp, z0, z1); unpk8(*(const u32x4*)(vf + row * 1024 + col0 + bj * HALF), f0, f1);
;                 const f32x4 m0 = act4(acc[ai][bj][m][0] + bv[bj][0], 2), m1 = act4(acc[ai][bj][m][1] + bv[bj][1], 2);
;                 *(u32x4*)zp = pk8(z0 + (f0 - z0) * m0, z1 + (f1 - z1) * m1); }
;         EPI_ROWS_END
	v_lshlrev_b32_e32 v58, 16, v54
	v_and_b32_e32 v59, 0xffff0000, v54
	v_lshlrev_b32_e32 v60, 16, v55
	v_and_b32_e32 v61, 0xffff0000, v55
	v_lshlrev_b32_e32 v66, 16, v62
	v_and_b32_e32 v62, 0xffff0000, v62
	v_lshlrev_b32_e32 v67, 16, v63
	v_and_b32_e32 v68, 0xffff0000, v63
	v_lshlrev_b32_e32 v54, 16, v56
	v_and_b32_e32 v55, 0xffff0000, v56
	v_lshlrev_b32_e32 v56, 16, v57
	v_and_b32_e32 v57, 0xffff0000, v57
	v_lshlrev_b32_e32 v69, 16, v64
	v_and_b32_e32 v70, 0xffff0000, v64
	v_lshlrev_b32_e32 v71, 16, v65
	v_and_b32_e32 v72, 0xffff0000, v65
	v_sub_f32_e32 v63, v62, v59
	v_sub_f32_e32 v62, v66, v58
	v_sub_f32_e32 v65, v68, v61
	v_sub_f32_e32 v64, v67, v60
	v_pk_fma_f32 v[48:49], v[48:49], v[64:65], v[60:61]
	v_pk_fma_f32 v[46:47], v[46:47], v[62:63], v[58:59]
	v_sub_f32_e32 v59, v70, v55
	v_sub_f32_e32 v58, v69, v54
	v_sub_f32_e32 v61, v72, v57
	v_sub_f32_e32 v60, v71, v56
	v_pk_fma_f32 v[56:57], v[40:41], v[60:61], v[56:57]
	v_pk_fma_f32 v[40:41], v[38:39], v[58:59], v[54:55]
	v_cvt_pk_bf16_f32 v38, v46, v47
	v_cvt_pk_bf16_f32 v39, v48, v49
	s_nop 0
	v_cvt_pk_bf16_f32 v40, v40, v41
	v_cvt_pk_bf16_f32 v41, v56, v57
	global_store_dwordx4 v[50:51], v[38:41], off
	v_lshlrev_b32_e32 v46, 16, v190
	v_and_b32_e32 v47, 0xffff0000, v190
	v_lshlrev_b32_e32 v48, 16, v191
	v_and_b32_e32 v49, 0xffff0000, v191
	v_lshlrev_b32_e32 v54, 16, v192
	v_and_b32_e32 v55, 0xffff0000, v192
	v_lshlrev_b32_e32 v56, 16, v193
	v_and_b32_e32 v57, 0xffff0000, v193
	v_lshlrev_b32_e32 v52, 16, v194
	v_and_b32_e32 v38, 0xffff0000, v194
	v_lshlrev_b32_e32 v53, 16, v195
	v_and_b32_e32 v58, 0xffff0000, v195
	v_lshlrev_b32_e32 v59, 16, v196
	v_and_b32_e32 v60, 0xffff0000, v196
	v_lshlrev_b32_e32 v61, 16, v197
	v_and_b32_e32 v62, 0xffff0000, v197
	v_sub_f32_e32 v39, v38, v47
	v_sub_f32_e32 v38, v52, v46
	v_sub_f32_e32 v41, v58, v49
	v_sub_f32_e32 v40, v53, v48
	v_pk_fma_f32 v[32:33], v[32:33], v[40:41], v[48:49]
	v_pk_fma_f32 v[30:31], v[30:31], v[38:39], v[46:47]
	v_sub_f32_e32 v39, v60, v55
	v_sub_f32_e32 v38, v59, v54
	v_sub_f32_e32 v41, v62, v57
	v_sub_f32_e32 v40, v61, v56
	v_pk_fma_f32 v[40:41], v[28:29], v[40:41], v[56:57]
	v_pk_fma_f32 v[28:29], v[26:27], v[38:39], v[54:55]
	v_cvt_pk_bf16_f32 v26, v30, v31
	v_cvt_pk_bf16_f32 v27, v32, v33
	s_nop 0
	v_cvt_pk_bf16_f32 v28, v28, v29
	v_cvt_pk_bf16_f32 v29, v40, v41
	global_store_dwordx4 v[50:51], v[26:29], off offset:256
	s_nop 1
	v_add_u32_e32 v26, 0xb0, v162
	v_ashrrev_i32_e32 v27, 31, v26
	v_lshlrev_b64 v[28:29], 11, v[26:27]
	v_mad_i64_i32 v[26:27], s[60:61], v26, s27, v[160:161]
	v_lshl_add_u64 v[26:27], v[26:27], 0, v[158:159]
	v_add_co_u32_e32 v26, vcc, s9, v26
	v_lshl_add_u64 v[28:29], s[56:57], 0, v[28:29]
	s_nop 0
	v_addc_co_u32_e32 v27, vcc, 0, v27, vcc
	v_lshl_add_u64 v[28:29], v[28:29], 0, v[158:159]
	global_load_dwordx4 v[30:33], v[26:27], off
	global_load_dwordx4 v[46:49], v[28:29], off
	global_load_dwordx4 v[190:193], v[26:27], off offset:256
	global_load_dwordx4 v[194:197], v[28:29], off offset:256
	s_mov_b64 s[60:61], -1
	s_and_b64 vcc, exec, s[36:37]
	s_waitcnt vmcnt(0)
	v_lshlrev_b32_e32 v38, 16, v30
	v_and_b32_e32 v39, 0xffff0000, v30
	v_lshlrev_b32_e32 v40, 16, v31
	v_and_b32_e32 v41, 0xffff0000, v31
	v_lshlrev_b32_e32 v50, 16, v46
	v_and_b32_e32 v46, 0xffff0000, v46
	v_lshlrev_b32_e32 v51, 16, v47
	v_and_b32_e32 v47, 0xffff0000, v47
	v_lshlrev_b32_e32 v30, 16, v32
	v_and_b32_e32 v31, 0xffff0000, v32
	v_lshlrev_b32_e32 v32, 16, v33
	v_and_b32_e32 v33, 0xffff0000, v33
	v_lshlrev_b32_e32 v52, 16, v48
	v_and_b32_e32 v48, 0xffff0000, v48
	v_lshlrev_b32_e32 v53, 16, v49
	v_and_b32_e32 v49, 0xffff0000, v49
	v_sub_f32_e32 v35, v46, v39
	v_sub_f32_e32 v34, v50, v38
	v_sub_f32_e32 v37, v47, v41
	v_sub_f32_e32 v36, v51, v40
	v_pk_fma_f32 v[16:17], v[16:17], v[36:37], v[40:41]
	v_pk_fma_f32 v[14:15], v[14:15], v[34:35], v[38:39]
	v_sub_f32_e32 v35, v48, v31
	v_sub_f32_e32 v34, v52, v30
	v_sub_f32_e32 v37, v49, v33
	v_sub_f32_e32 v36, v53, v32
	v_pk_fma_f32 v[32:33], v[12:13], v[36:37], v[32:33]
	v_pk_fma_f32 v[12:13], v[10:11], v[34:35], v[30:31]
	v_cvt_pk_bf16_f32 v10, v14, v15
	v_cvt_pk_bf16_f32 v11, v16, v17
	s_nop 0
	v_cvt_pk_bf16_f32 v12, v12, v13
	v_cvt_pk_bf16_f32 v13, v32, v33
	global_store_dwordx4 v[26:27], v[10:13], off
	v_lshlrev_b32_e32 v14, 16, v190
	v_and_b32_e32 v15, 0xffff0000, v190
	v_lshlrev_b32_e32 v16, 16, v191
	v_and_b32_e32 v17, 0xffff0000, v191
	v_lshlrev_b32_e32 v30, 16, v192
	v_and_b32_e32 v31, 0xffff0000, v192
	v_lshlrev_b32_e32 v32, 16, v193
	v_and_b32_e32 v33, 0xffff0000, v193
	v_lshlrev_b32_e32 v28, 16, v194
	v_and_b32_e32 v10, 0xffff0000, v194
	v_lshlrev_b32_e32 v29, 16, v195
	v_and_b32_e32 v34, 0xffff0000, v195
	v_lshlrev_b32_e32 v35, 16, v196
	v_and_b32_e32 v36, 0xffff0000, v196
	v_lshlrev_b32_e32 v37, 16, v197
	v_and_b32_e32 v38, 0xffff0000, v197
	v_sub_f32_e32 v11, v10, v15
	v_sub_f32_e32 v10, v28, v14
	v_sub_f32_e32 v13, v34, v17
	v_sub_f32_e32 v12, v29, v16
	v_pk_fma_f32 v[8:9], v[8:9], v[12:13], v[16:17]
	v_pk_fma_f32 v[6:7], v[6:7], v[10:11], v[14:15]
	v_sub_f32_e32 v11, v36, v31
	v_sub_f32_e32 v10, v35, v30
	v_sub_f32_e32 v13, v38, v33
	v_sub_f32_e32 v12, v37, v32
	v_pk_fma_f32 v[12:13], v[4:5], v[12:13], v[32:33]
	v_pk_fma_f32 v[4:5], v[2:3], v[10:11], v[30:31]
	v_cvt_pk_bf16_f32 v2, v6, v7
	v_cvt_pk_bf16_f32 v3, v8, v9
	s_nop 0
	v_cvt_pk_bf16_f32 v4, v4, v5
	v_cvt_pk_bf16_f32 v5, v12, v13
	global_store_dwordx4 v[26:27], v[2:5], off offset:256
	s_cbranch_vccnz .LBB0_750
	s_andn2_b64 vcc, exec, s[44:45]
	s_cbranch_vccnz .LBB0_749
	s_barrier
	s_branch .LBB0_749
